# acquire buffer_inv issued before the first flag poll instead of after the spin (9 wait sites)
# speedup vs baseline: 1.1804x; 1.1804x over previous
.LBB0_394:
	s_or_b64 exec, exec, s[4:5]
	s_lshl_b32 s4, s89, 6
	s_add_u32 s4, s46, s4
	s_addc_u32 s5, s47, 0
	v_mov_b32_e32 v1, 0xe000
	buffer_inv sc1
	global_load_dword v1, v1, s[4:5] offset:2304 sc1
	s_add_u32 s4, s4, 0xe900
	s_addc_u32 s5, s5, 0
	s_waitcnt vmcnt(0)
	v_cmp_ne_u32_e32 vcc, 0, v1
	s_cbranch_vccnz .LBB0_407
	s_mov_b32 s12, 1
	v_mov_b32_e32 v1, 0
	s_branch .LBB0_397

.LBB0_406:
	s_or_b64 exec, exec, s[4:5]
.LBB0_407:
	s_waitcnt vmcnt(0)
	s_waitcnt vmcnt(0)
.LBB0_408:
	s_or_b64 exec, exec, s[0:1]
	s_waitcnt lgkmcnt(0)
	s_barrier

.LBB0_464:
	s_and_b64 vcc, exec, s[42:43]
	s_cbranch_vccnz .LBB0_483
	s_and_saveexec_b64 s[0:1], s[40:41]
	s_cbranch_execz .LBB0_482
	s_lshl_b32 s4, s89, 6
	s_add_u32 s4, s46, s4
	s_addc_u32 s5, s47, 0
	v_mov_b32_e32 v2, 0xf000
	buffer_inv sc1
	global_load_dword v2, v2, s[4:5] offset:2304 sc1
	s_add_u32 s4, s4, 0xf900
	s_addc_u32 s5, s5, 0
	s_waitcnt vmcnt(0)
	v_cmp_ne_u32_e32 vcc, 0, v2
	s_cbranch_vccnz .LBB0_481
	s_mov_b32 s16, 1
	v_mov_b32_e32 v2, 0
	s_branch .LBB0_469

.LBB0_481:
	s_waitcnt vmcnt(0) lgkmcnt(0)
	s_waitcnt vmcnt(0)

.LBB0_796:
	s_cmp_lt_i32 s52, 4
	s_cselect_b64 s[0:1], -1, 0
	s_cmp_gt_i32 s53, 3
	s_cselect_b64 s[4:5], -1, 0
	s_and_b64 s[8:9], s[0:1], s[4:5]
	s_andn2_b64 vcc, exec, s[8:9]
	s_cbranch_vccnz .LBB0_1193
	s_and_b64 vcc, exec, s[42:43]
	s_cbranch_vccnz .LBB0_814
	s_and_saveexec_b64 s[0:1], s[40:41]
	s_cbranch_execz .LBB0_813
	s_lshl_b32 s4, s89, 6
	s_add_u32 s4, s46, s4
	s_addc_u32 s5, s47, 0
	v_mov_b32_e32 v1, 0x8000
	buffer_inv sc1
	global_load_dword v1, v1, s[4:5] offset:2304 sc1
	s_add_u32 s4, s4, 0x8900
	s_addc_u32 s5, s5, 0
	s_waitcnt vmcnt(0)
	v_cmp_ne_u32_e32 vcc, 0, v1
	s_cbranch_vccnz .LBB0_812
	s_mov_b32 s14, 1
	v_mov_b32_e32 v1, 0
	s_branch .LBB0_802

.LBB0_1147:
	s_or_b64 exec, exec, s[6:7]
	s_lshl_b32 s6, s89, 6
	s_add_u32 s6, s46, s6
	s_addc_u32 s7, s47, 0
	v_mov_b32_e32 v1, 0x9000
	buffer_inv sc1
	global_load_dword v1, v1, s[6:7] offset:2304 sc1
	s_add_u32 s6, s6, 0x9900
	s_addc_u32 s7, s7, 0
	s_waitcnt vmcnt(0)
	v_cmp_ne_u32_e32 vcc, 0, v1
	s_cbranch_vccnz .LBB0_1160
	s_mov_b32 s16, 1
	v_mov_b32_e32 v1, 0
	s_branch .LBB0_1150

.LBB0_1159:
	s_or_b64 exec, exec, s[6:7]
.LBB0_1160:
	s_waitcnt vmcnt(0)
	s_waitcnt vmcnt(0)
.LBB0_1161:
	s_or_b64 exec, exec, s[4:5]
	s_waitcnt lgkmcnt(0)
	s_barrier

.LBB0_1290:
	s_add_u32 s70, s46, 0xc000000
	s_addc_u32 s71, s47, 0
	s_cmp_lt_i32 s52, 5
	s_cselect_b64 s[0:1], -1, 0
	s_cmp_gt_i32 s53, 4
	s_cselect_b64 s[4:5], -1, 0
	s_and_b64 s[72:73], s[0:1], s[4:5]
	s_andn2_b64 vcc, exec, s[72:73]
	s_cbranch_vccnz .LBB0_1302
	s_and_b64 vcc, exec, s[42:43]
	s_cbranch_vccnz .LBB0_1321
	s_and_saveexec_b64 s[0:1], s[40:41]
	s_cbranch_execz .LBB0_1320
	s_lshl_b32 s4, s89, 6
	s_add_u32 s4, s46, s4
	s_addc_u32 s5, s47, 0
	v_mov_b32_e32 v1, 0xa000
	buffer_inv sc1
	global_load_dword v1, v1, s[4:5] offset:2304 sc1
	s_add_u32 s4, s4, 0xa900
	s_addc_u32 s5, s5, 0
	s_waitcnt vmcnt(0)
	v_cmp_ne_u32_e32 vcc, 0, v1
	s_cbranch_vccnz .LBB0_1319
	s_mov_b32 s12, 1
	v_mov_b32_e32 v1, 0
	s_branch .LBB0_1296

.LBB0_1393:
	s_waitcnt lgkmcnt(0)
	s_barrier
	s_and_b64 vcc, exec, s[42:43]
	s_cbranch_vccnz .LBB0_1410
	s_and_saveexec_b64 s[0:1], s[40:41]
	s_cbranch_execz .LBB0_1409
	s_lshl_b32 s4, s89, 6
	s_add_u32 s4, s46, s4
	s_addc_u32 s5, s47, 0
	v_mov_b32_e32 v2, 0xb000
	buffer_inv sc1
	global_load_dword v2, v2, s[4:5] offset:2304 sc1
	s_add_u32 s4, s4, 0xb900
	s_addc_u32 s5, s5, 0
	s_waitcnt vmcnt(0)
	v_cmp_ne_u32_e32 vcc, 0, v2
	s_cbranch_vccnz .LBB0_1408
	s_mov_b32 s12, 1
	v_mov_b32_e32 v2, 0
	s_branch .LBB0_1398

.LBB0_1580:
	ds_bpermute_b32 v228, v1, v162
	s_and_b64 vcc, exec, s[42:43]
	s_cbranch_vccnz .LBB0_1597
	s_and_saveexec_b64 s[78:79], s[40:41]
	s_cbranch_execz .LBB0_1596
	buffer_inv sc1
	global_load_dword v66, v163, s[68:69] sc1
	s_waitcnt vmcnt(0)
	v_cmp_ne_u32_e32 vcc, 0, v66
	s_cbranch_vccnz .LBB0_1595
	s_mov_b32 s33, 1
	s_branch .LBB0_1585

.LBB0_1855:
	s_andn2_b64 vcc, exec, s[4:5]
	s_cbranch_vccnz .LBB0_1919
	v_lshlrev_b32_e32 v1, 4, v0
	s_waitcnt lgkmcnt(0)
	v_and_b32_e32 v2, 32, v0
	v_bitop3_b32 v1, v1, v2, 48 bitop3:0x6c
	v_lshrrev_b32_e32 v2, 1, v0
	v_and_b32_e32 v10, 24, v2
	v_lshrrev_b32_e32 v2, 5, v0
	v_and_b32_e32 v2, 4, v2
	v_bfe_u32 v3, v0, 2, 2
	v_or3_b32 v4, v2, v3, v10
	v_lshrrev_b32_e32 v2, 3, v0
	s_lshr_b32 s15, s14, 6
	v_and_or_b32 v1, v0, 64, v1
	v_and_or_b32 v3, v2, 32, v4
	s_lshl_b32 s49, s15, 10
	v_lshl_or_b32 v130, v3, 11, v1
	v_bfe_u32 v3, v0, 3, 25
	s_add_u32 s54, s46, 0x900000
	v_or_b32_e32 v3, 64, v3
	s_movk_i32 s4, 0x60
	s_addc_u32 s55, s47, 0
	v_and_or_b32 v4, v3, s4, v4
	s_and_b64 s[4:5], s[58:59], exec
	s_cselect_b32 s80, 12, 0
	s_ashr_i32 s31, s30, 31
	s_xor_b64 s[4:5], s[58:59], -1
	s_lshl_b64 s[8:9], s[30:31], 19
	s_add_u32 s36, s54, s8
	s_addc_u32 s37, s55, s9
	s_add_i32 s31, s49, 0
	s_add_i32 m0, s31, 0x10000
	v_lshl_or_b32 v132, v4, 11, v1
	global_load_lds_dwordx4 v130, s[36:37]
	s_add_i32 m0, s31, 0x12000
	s_add_u32 s8, s36, 0x40000
	global_load_lds_dwordx4 v132, s[36:37]
	s_addc_u32 s9, s37, 0
	s_add_i32 m0, s31, 0x14000
	s_waitcnt vmcnt(0)
	v_mov_b32_e32 v135, 0
	global_load_lds_dwordx4 v130, s[8:9]
	s_add_i32 m0, s31, 0x16000
	s_cmp_gt_i32 s30, 3
	global_load_lds_dwordx4 v132, s[8:9]
	s_cselect_b64 s[8:9], -1, 0
	s_or_b64 s[4:5], s[4:5], s[8:9]
	v_lshrrev_b32_e32 v4, 2, v0
	v_mov_b32_e32 v131, v135
	v_mov_b32_e32 v133, v135
	s_and_b64 vcc, exec, s[4:5]
	s_cbranch_vccnz .LBB0_1873
	s_and_saveexec_b64 s[4:5], s[40:41]
	s_cbranch_execz .LBB0_1872
	v_mov_b32_e32 v5, 0
	buffer_inv sc1
	global_load_dword v6, v5, s[64:65] sc1
	s_waitcnt vmcnt(0)
	v_cmp_le_u32_e32 vcc, s80, v6
	s_cbranch_vccnz .LBB0_1871
	s_mov_b32 s16, 1
	s_branch .LBB0_1861

.LBB0_2124:
	s_andn2_b64 vcc, exec, s[0:1]
	s_cbranch_vccnz .LBB0_2174
	v_lshlrev_b32_e32 v1, 4, v0
	v_and_b32_e32 v2, 32, v0
	v_bitop3_b32 v1, v1, v2, 48 bitop3:0x6c
	v_and_or_b32 v2, v0, 64, v1
	v_lshrrev_b32_e32 v1, 1, v0
	v_lshrrev_b32_e32 v3, 5, v0
	v_and_b32_e32 v1, 24, v1
	v_and_b32_e32 v3, 4, v3
	v_bfe_u32 v4, v0, 2, 2
	s_add_u32 s33, s46, 0x1900000
	v_or3_b32 v5, v3, v4, v1
	v_lshrrev_b32_e32 v3, 3, v0
	s_addc_u32 s52, s47, 0
	v_and_or_b32 v4, v3, 32, v5
	s_and_b64 s[0:1], s[58:59], exec
	v_lshl_or_b32 v168, v4, 11, v2
	v_bfe_u32 v4, v0, 3, 25
	s_cselect_b32 s53, 20, 0
	v_or_b32_e32 v4, 64, v4
	s_movk_i32 s4, 0x60
	s_lshr_b32 s12, s49, 6
	s_ashr_i32 s23, s22, 31
	s_xor_b64 s[0:1], s[58:59], -1
	v_and_or_b32 v5, v4, s4, v5
	s_lshl_b32 s54, s12, 10
	s_lshl_b64 s[4:5], s[22:23], 19
	s_add_u32 s26, s33, s4
	s_addc_u32 s27, s52, s5
	s_add_i32 s23, s54, 0
	s_add_i32 m0, s23, 0x10000
	v_lshl_or_b32 v170, v5, 11, v2
	global_load_lds_dwordx4 v168, s[26:27]
	s_add_i32 m0, s23, 0x12000
	s_add_u32 s4, s26, 0x40000
	global_load_lds_dwordx4 v170, s[26:27]
	s_addc_u32 s5, s27, 0
	s_add_i32 m0, s23, 0x14000
	v_mov_b32_e32 v173, 0
	global_load_lds_dwordx4 v168, s[4:5]
	s_add_i32 m0, s23, 0x16000
	s_cmp_gt_i32 s22, 3
	global_load_lds_dwordx4 v170, s[4:5]
	s_cselect_b64 s[4:5], -1, 0
	s_or_b64 s[0:1], s[0:1], s[4:5]
	v_lshrrev_b32_e32 v5, 2, v0
	v_mov_b32_e32 v169, v173
	v_mov_b32_e32 v171, v173
	s_and_b64 vcc, exec, s[0:1]
	s_cbranch_vccnz .LBB0_2142
	s_and_saveexec_b64 s[0:1], s[40:41]
	s_cbranch_execz .LBB0_2141
	v_mov_b32_e32 v6, 0
	buffer_inv sc1
	global_load_dword v7, v6, s[64:65] sc1
	s_waitcnt vmcnt(0)
	v_cmp_le_u32_e32 vcc, s53, v7
	s_cbranch_vccnz .LBB0_2140
	s_mov_b32 s13, 1
	s_branch .LBB0_2130
